# P5: next-unit prefetch issued after the unit's own loads, packed at unit end (one exposed round trip less per unit); plus grid-barrier leader reorder
# speedup vs baseline: 1.0273x; 1.0096x over previous
.LBB0_87:
	s_or_b64 exec, exec, s[8:9]
	s_mov_b64 s[8:9], exec
	v_mbcnt_lo_u32_b32 v1, s8, 0
	v_mbcnt_hi_u32_b32 v1, s9, v1
	v_cmp_eq_u32_e32 vcc, 0, v1
	s_and_saveexec_b64 s[10:11], vcc
	s_cbranch_execz .LBB0_89
	s_bcnt1_i32_b64 s8, s[8:9]
	v_mov_b32_e32 v1, 0x2000
	v_mov_b32_e32 v2, s8
	global_atomic_add v1, v2, s[6:7] offset:1024
.LBB0_89:
	s_or_b64 exec, exec, s[10:11]
	s_waitcnt vmcnt(0)
	buffer_inv sc1
	s_waitcnt vmcnt(0)
.LBB0_90:
	s_or_b64 exec, exec, s[0:1]
	s_waitcnt lgkmcnt(0)
	s_barrier

.LBB0_173:
	s_or_b64 exec, exec, s[10:11]
	s_waitcnt vmcnt(0)
	buffer_inv sc1
	s_waitcnt vmcnt(0)
.LBB0_174:
	s_or_b64 exec, exec, s[0:1]
	s_waitcnt lgkmcnt(0)
	s_barrier

.LBB0_332:
	s_or_b64 exec, exec, s[6:7]
	v_mov_b32_e32 v1, 0x2000
	v_mov_b32_e32 v2, 1
	global_atomic_add v1, v2, s[4:5] offset:1024
	s_waitcnt vmcnt(0)
	buffer_inv sc1
	s_waitcnt vmcnt(0)

.LBB0_516:
	s_or_b64 exec, exec, s[6:7]
	s_mov_b64 s[6:7], exec
	v_mbcnt_lo_u32_b32 v1, s6, 0
	v_mbcnt_hi_u32_b32 v1, s7, v1
	v_cmp_eq_u32_e32 vcc, 0, v1
	s_and_saveexec_b64 s[8:9], vcc
	s_cbranch_execz .LBB0_518
	s_bcnt1_i32_b64 s3, s[6:7]
	v_mov_b32_e32 v1, 0x2000
	v_mov_b32_e32 v2, s3
	global_atomic_add v1, v2, s[4:5] offset:1024
.LBB0_518:
	s_or_b64 exec, exec, s[8:9]
	s_waitcnt vmcnt(0)
	buffer_inv sc1
	s_waitcnt vmcnt(0)
.LBB0_519:
	s_or_b64 exec, exec, s[0:1]
	s_waitcnt lgkmcnt(0)
	s_barrier

.LBB0_523:
	v_perm_b32 v133, v133, v226, s73
	v_perm_b32 v132, v132, v234, s73
	v_perm_b32 v2, v2, v242, s73
	v_perm_b32 v135, v135, v227, s73
	v_perm_b32 v134, v134, v235, s73
	v_perm_b32 v1, v1, v243, s73
	v_perm_b32 v137, v137, v228, s73
	v_perm_b32 v136, v136, v236, s73
	v_perm_b32 v4, v4, v244, s73
	v_perm_b32 v139, v139, v229, s73
	v_perm_b32 v138, v138, v237, s73
	v_perm_b32 v3, v3, v245, s73
	v_perm_b32 v141, v141, v230, s73
	v_perm_b32 v140, v140, v238, s73
	v_perm_b32 v6, v6, v246, s73
	v_perm_b32 v143, v143, v231, s73
	v_perm_b32 v142, v142, v239, s73
	v_perm_b32 v5, v5, v247, s73
	v_perm_b32 v145, v145, v232, s73
	v_perm_b32 v144, v144, v240, s73
	v_perm_b32 v8, v8, v248, s73
	v_perm_b32 v147, v147, v233, s73
	v_perm_b32 v146, v146, v241, s73
	v_perm_b32 v7, v7, v249, s73
	v_mov_b64_e32 v[48:49], v[24:25]
	v_mov_b64_e32 v[44:45], v[20:21]
	v_mov_b64_e32 v[40:41], v[16:17]
	v_mov_b64_e32 v[36:37], v[12:13]
	s_andn2_b64 vcc, exec, s[68:69]
	v_mov_b32_e32 v33, v7
	v_mov_b32_e32 v32, v8
	v_mov_b32_e32 v31, v5
	v_mov_b32_e32 v30, v6
	v_mov_b32_e32 v29, v3
	v_mov_b32_e32 v28, v4
	v_mov_b32_e32 v27, v1
	v_mov_b32_e32 v26, v2
	v_mov_b64_e32 v[46:47], v[22:23]
	v_mov_b64_e32 v[42:43], v[18:19]
	v_mov_b64_e32 v[38:39], v[14:15]
	v_mov_b64_e32 v[34:35], v[10:11]
	s_mov_b32 s61, s92
	s_mov_b32 s91, s93
	v_mov_b32_e32 v160, v133
	v_mov_b32_e32 v159, v135
	v_mov_b32_e32 v158, v137
	v_mov_b32_e32 v157, v139
	v_mov_b32_e32 v156, v141
	v_mov_b32_e32 v155, v143
	v_mov_b32_e32 v154, v145
	v_mov_b32_e32 v153, v147
	v_mov_b32_e32 v152, v132
	v_mov_b32_e32 v151, v134
	v_mov_b32_e32 v150, v136
	v_mov_b32_e32 v149, v138
	v_mov_b32_e32 v148, v140
	v_mov_b32_e32 v69, v142
	v_mov_b32_e32 v68, v144
	v_mov_b32_e32 v67, v146
	s_cbranch_vccz .LBB0_539

.LBB0_526:
	s_ashr_i32 s80, s61, 10
	s_ashr_i32 s81, s80, 31
	s_lshl_b32 s42, s61, 6
	s_lshl_b64 s[82:83], s[80:81], 13
	s_and_b32 s94, s42, 0x1fc0
	s_or_b32 s65, s82, s94
	v_or_b32_e32 v108, s65, v84
	v_mov_b64_e32 v[102:103], s[76:77]
	s_and_b32 s84, s61, 0x380
	v_mad_u64_u32 v[110:111], vcc, v108, s3, v[102:103]
	v_mov_b32_e32 v101, s83
	v_or_b32_e32 v100, s65, v72
	s_lshl_b32 s42, s84, 1
	v_mad_i32_i24 v111, s83, v73, v111
	v_lshlrev_b64 v[50:51], 12, v[100:101]
	v_lshl_add_u64 v[102:103], v[110:111], 0, s[42:43]
	v_mov_b32_e32 v97, v75
	v_lshl_add_u64 v[50:51], s[48:49], 0, v[50:51]
	v_mov_b32_e32 v9, s83
	v_lshl_add_u64 v[102:103], v[102:103], 0, v[96:97]
	s_mov_b64 s[82:83], 0x364eb000
	v_or_b32_e32 v66, s84, v70
	v_lshl_add_u64 v[50:51], v[50:51], 0, s[42:43]
	v_lshlrev_b64 v[58:59], 5, v[100:101]
	v_lshl_add_u64 v[102:103], v[102:103], 0, s[82:83]
	s_mov_b32 s61, s43
	v_lshlrev_b32_e32 v162, 2, v66
	v_mov_b32_e32 v163, v75
	v_lshl_add_u64 v[54:55], v[50:51], 0, v[74:75]
	v_lshl_add_u64 v[62:63], s[54:55], 0, v[58:59]
	v_lshl_add_u64 v[104:105], v[102:103], 0, s[60:61]
	v_lshl_add_u64 v[164:165], s[38:39], 0, v[162:163]
	global_load_dwordx4 v[50:53], v[54:55], off offset:16
	s_nop 0
	global_load_dwordx4 v[54:57], v[54:55], off
	s_nop 0
	global_load_dwordx4 v[58:61], v[62:63], off offset:16
	s_nop 0
	global_load_dwordx4 v[62:65], v[62:63], off
	s_nop 0
	global_load_dwordx2 v[112:113], v[104:105], off
	global_load_dwordx2 v[106:107], v[104:105], off offset:32
	s_nop 0
	global_load_dwordx2 v[104:105], v[104:105], off offset:64
	s_mov_b32 s65, s43
	global_load_dword v66, v162, s[38:39]
	v_add_co_u32_e32 v162, vcc, s72, v164
	v_lshl_add_u64 v[102:103], v[102:103], 0, s[64:65]
	s_nop 0
	v_addc_co_u32_e32 v163, vcc, 0, v165, vcc
	global_load_dword v97, v[162:163], off
	s_andn2_b64 vcc, exec, s[56:57]
	global_load_dwordx2 v[102:103], v[102:103], off
	s_waitcnt vmcnt(1)
	s_cmp_lg_u64 s[68:69], 0
	s_cbranch_scc1 .Lp5pf_done
	s_ashr_i32 s100, s92, 10
	s_lshl_b32 s98, s92, 6
	s_ashr_i32 s101, s100, 31
	s_and_b32 s98, s98, 0x1fc0
	s_lshl_b64 s[100:101], s[100:101], 13
	v_or_b32_e32 v252, s98, v71
	v_or_b32_e32 v252, s100, v252
	v_mov_b64_e32 v[250:251], s[0:1]
	s_and_b32 s98, s92, 0x380
	s_lshl_b32 s98, s98, 1
	s_addk_i32 s98, 0x2000
	s_mov_b32 s99, 0
	v_mad_u64_u32 v[250:251], s[82:83], v252, s3, v[250:251]
	v_lshlrev_b32_e32 v226, 1, v70
	v_mov_b32_e32 v227, v75
	v_mad_i32_i24 v251, s101, v73, v251
	v_lshl_add_u64 v[226:227], v[226:227], 0, s[98:99]
	s_ashr_i32 s101, s92, 31
	s_mov_b32 s100, s92
	v_lshl_add_u64 v[250:251], v[250:251], 0, v[226:227]
	s_lshl_b64 s[100:101], s[100:101], 15
	s_movk_i32 s98, 0x3800
	global_load_ushort v234, v[250:251], off offset:-2048
	global_load_ushort v226, v[250:251], off
	global_load_ushort v242, v[250:251], off offset:2048
	v_lshl_add_u64 v[250:251], v[250:251], 0, s[98:99]
	global_load_ushort v132, v[250:251], off offset:-2048
	global_load_ushort v133, v[250:251], off
	global_load_ushort v2, v[250:251], off offset:2048
	v_lshl_add_u64 v[250:251], v[250:251], 0, s[98:99]
	global_load_ushort v235, v[250:251], off offset:-2048
	global_load_ushort v227, v[250:251], off
	global_load_ushort v243, v[250:251], off offset:2048
	v_lshl_add_u64 v[250:251], v[250:251], 0, s[98:99]
	global_load_ushort v134, v[250:251], off offset:-2048
	global_load_ushort v135, v[250:251], off
	global_load_ushort v1, v[250:251], off offset:2048
	v_lshl_add_u64 v[250:251], v[250:251], 0, s[98:99]
	global_load_ushort v236, v[250:251], off offset:-2048
	global_load_ushort v228, v[250:251], off
	global_load_ushort v244, v[250:251], off offset:2048
	v_lshl_add_u64 v[250:251], v[250:251], 0, s[98:99]
	global_load_ushort v136, v[250:251], off offset:-2048
	global_load_ushort v137, v[250:251], off
	global_load_ushort v4, v[250:251], off offset:2048
	v_lshl_add_u64 v[250:251], v[250:251], 0, s[98:99]
	global_load_ushort v237, v[250:251], off offset:-2048
	global_load_ushort v229, v[250:251], off
	global_load_ushort v245, v[250:251], off offset:2048
	v_lshl_add_u64 v[250:251], v[250:251], 0, s[98:99]
	global_load_ushort v138, v[250:251], off offset:-2048
	global_load_ushort v139, v[250:251], off
	global_load_ushort v3, v[250:251], off offset:2048
	v_lshl_add_u64 v[250:251], v[250:251], 0, s[98:99]
	global_load_ushort v238, v[250:251], off offset:-2048
	global_load_ushort v230, v[250:251], off
	global_load_ushort v246, v[250:251], off offset:2048
	v_lshl_add_u64 v[250:251], v[250:251], 0, s[98:99]
	global_load_ushort v140, v[250:251], off offset:-2048
	global_load_ushort v141, v[250:251], off
	global_load_ushort v6, v[250:251], off offset:2048
	v_lshl_add_u64 v[250:251], v[250:251], 0, s[98:99]
	global_load_ushort v239, v[250:251], off offset:-2048
	global_load_ushort v231, v[250:251], off
	global_load_ushort v247, v[250:251], off offset:2048
	v_lshl_add_u64 v[250:251], v[250:251], 0, s[98:99]
	global_load_ushort v142, v[250:251], off offset:-2048
	global_load_ushort v143, v[250:251], off
	global_load_ushort v5, v[250:251], off offset:2048
	v_lshl_add_u64 v[250:251], v[250:251], 0, s[98:99]
	global_load_ushort v240, v[250:251], off offset:-2048
	global_load_ushort v232, v[250:251], off
	global_load_ushort v248, v[250:251], off offset:2048
	v_lshl_add_u64 v[250:251], v[250:251], 0, s[98:99]
	global_load_ushort v144, v[250:251], off offset:-2048
	global_load_ushort v145, v[250:251], off
	global_load_ushort v8, v[250:251], off offset:2048
	v_lshl_add_u64 v[250:251], v[250:251], 0, s[98:99]
	global_load_ushort v241, v[250:251], off offset:-2048
	global_load_ushort v233, v[250:251], off
	global_load_ushort v249, v[250:251], off offset:2048
	v_lshl_add_u64 v[250:251], v[250:251], 0, s[98:99]
	global_load_ushort v146, v[250:251], off offset:-2048
	global_load_ushort v147, v[250:251], off
	global_load_ushort v7, v[250:251], off offset:2048
	v_lshl_add_u64 v[10:11], v[82:83], 0, s[100:101]
	s_mov_b32 s100, s86
	s_mov_b32 s101, 0
	v_lshl_add_u64 v[14:15], v[10:11], 0, v[78:79]
	v_lshl_add_u64 v[22:23], v[10:11], 0, v[80:81]
	v_lshl_add_u64 v[10:11], v[10:11], 0, v[76:77]
	v_lshl_add_u64 v[18:19], v[10:11], 0, s[100:101]
	global_load_dwordx4 v[22:25], v[22:23], off
	global_load_dwordx4 v[14:17], v[14:15], off
	global_load_dwordx4 v[18:21], v[18:19], off
	global_load_dwordx4 v[10:13], v[10:11], off
.Lp5pf_done:
	v_sub_f32_e32 v66, v97, v66
	v_mul_f32_e32 v66, 0x3fb8aa3b, v66
	v_exp_f32_e32 v66, v66
	s_nop 0
	v_add_f32_e32 v66, 1.0, v66
	v_rcp_f32_e32 v97, v66
	v_lshlrev_b32_e32 v66, 16, v160
	v_mul_f32_e32 v66, 0xbfb8aa3b, v66
	v_and_b32_e32 v160, 0xffff0000, v160
	v_exp_f32_e32 v66, v66
	v_mul_f32_e32 v160, 0xbfb8aa3b, v160
	v_exp_f32_e32 v160, v160
	v_sub_f32_e32 v170, 1.0, v97
	v_add_f32_e32 v66, 1.0, v66
	v_rcp_f32_e32 v66, v66
	v_add_f32_e32 v160, 1.0, v160
	v_rcp_f32_e32 v160, v160
	v_fma_f32 v167, v66, v170, v97
	v_log_f32_e32 v161, v167
	v_fma_f32 v165, v160, v170, v97
	v_log_f32_e32 v160, v165
	v_sub_f32_e32 v167, 1.0, v167
	v_add_f32_e32 v166, 0, v161
	v_sub_f32_e32 v165, 1.0, v165
	v_add_f32_e32 v172, v160, v166
	v_lshlrev_b32_e32 v160, 16, v159
	v_mul_f32_e32 v160, 0xbfb8aa3b, v160
	v_and_b32_e32 v159, 0xffff0000, v159
	v_exp_f32_e32 v160, v160
	v_mul_f32_e32 v159, 0xbfb8aa3b, v159
	v_exp_f32_e32 v159, v159
	v_mov_b32_e32 v66, 0
	v_add_f32_e32 v160, 1.0, v160
	v_rcp_f32_e32 v160, v160
	v_add_f32_e32 v159, 1.0, v159
	v_rcp_f32_e32 v159, v159
	v_fma_f32 v163, v160, v170, v97
	v_log_f32_e32 v160, v163
	v_fma_f32 v161, v159, v170, v97
	v_log_f32_e32 v159, v161
	v_sub_f32_e32 v163, 1.0, v163
	v_add_f32_e32 v173, v160, v172
	v_add_f32_e32 v174, v159, v173
	v_lshlrev_b32_e32 v159, 16, v158
	v_mul_f32_e32 v159, 0xbfb8aa3b, v159
	v_exp_f32_e32 v159, v159
	v_and_b32_e32 v158, 0xffff0000, v158
	v_mul_f32_e32 v158, 0xbfb8aa3b, v158
	v_exp_f32_e32 v158, v158
	v_add_f32_e32 v159, 1.0, v159
	v_rcp_f32_e32 v159, v159
	v_add_f32_e32 v158, 1.0, v158
	v_rcp_f32_e32 v158, v158
	v_fma_f32 v160, v159, v170, v97
	v_log_f32_e32 v159, v160
	v_fma_f32 v158, v158, v170, v97
	v_add_f32_e32 v175, v159, v174
	v_log_f32_e32 v159, v158
	s_nop 0
	v_add_f32_e32 v176, v159, v175
	v_lshlrev_b32_e32 v159, 16, v157
	v_mul_f32_e32 v159, 0xbfb8aa3b, v159
	v_exp_f32_e32 v159, v159
	v_and_b32_e32 v157, 0xffff0000, v157
	v_mul_f32_e32 v157, 0xbfb8aa3b, v157
	v_exp_f32_e32 v157, v157
	v_add_f32_e32 v159, 1.0, v159
	v_rcp_f32_e32 v159, v159
	v_add_f32_e32 v157, 1.0, v157
	v_rcp_f32_e32 v157, v157
	v_fma_f32 v159, v159, v170, v97
	v_log_f32_e32 v162, v159
	v_fma_f32 v171, v157, v170, v97
	v_log_f32_e32 v157, v171
	v_add_f32_e32 v177, v162, v176
	v_lshlrev_b32_e32 v162, 16, v156
	v_mul_f32_e32 v162, 0xbfb8aa3b, v162
	v_and_b32_e32 v156, 0xffff0000, v156
	v_exp_f32_e32 v162, v162
	v_mul_f32_e32 v156, 0xbfb8aa3b, v156
	v_exp_f32_e32 v156, v156
	v_add_f32_e32 v157, v157, v177
	v_add_f32_e32 v162, 1.0, v162
	v_rcp_f32_e32 v162, v162
	v_add_f32_e32 v156, 1.0, v156
	v_rcp_f32_e32 v156, v156
	v_fma_f32 v169, v162, v170, v97
	v_log_f32_e32 v162, v169
	v_fma_f32 v168, v156, v170, v97
	v_log_f32_e32 v156, v168
	v_add_f32_e32 v180, v162, v157
	v_add_f32_e32 v181, v156, v180
	v_lshlrev_b32_e32 v156, 16, v155
	v_mul_f32_e32 v156, 0xbfb8aa3b, v156
	v_and_b32_e32 v155, 0xffff0000, v155
	v_exp_f32_e32 v156, v156
	v_mul_f32_e32 v155, 0xbfb8aa3b, v155
	v_exp_f32_e32 v155, v155
	v_add_f32_e32 v156, 1.0, v156
	v_rcp_f32_e32 v156, v156
	v_add_f32_e32 v155, 1.0, v155
	v_rcp_f32_e32 v155, v155
	v_fma_f32 v164, v156, v170, v97
	v_log_f32_e32 v156, v164
	v_fma_f32 v162, v155, v170, v97
	v_log_f32_e32 v155, v162
	v_add_f32_e32 v182, v156, v181
	v_add_f32_e32 v183, v155, v182
	v_lshlrev_b32_e32 v155, 16, v154
	v_mul_f32_e32 v155, 0xbfb8aa3b, v155
	v_exp_f32_e32 v155, v155
	v_and_b32_e32 v154, 0xffff0000, v154
	v_mul_f32_e32 v154, 0xbfb8aa3b, v154
	v_exp_f32_e32 v154, v154
	v_add_f32_e32 v155, 1.0, v155
	v_rcp_f32_e32 v155, v155
	v_add_f32_e32 v154, 1.0, v154
	v_rcp_f32_e32 v154, v154
	v_fma_f32 v156, v155, v170, v97
	v_log_f32_e32 v155, v156
	s_nop 0
	v_add_f32_e32 v184, v155, v183
	v_fma_f32 v155, v154, v170, v97
	v_log_f32_e32 v154, v155
	s_nop 0
	v_add_f32_e32 v185, v154, v184
	v_lshlrev_b32_e32 v154, 16, v153
	v_mul_f32_e32 v154, 0xbfb8aa3b, v154
	v_and_b32_e32 v153, 0xffff0000, v153
	v_exp_f32_e32 v154, v154
	v_mul_f32_e32 v153, 0xbfb8aa3b, v153
	v_exp_f32_e32 v153, v153
	v_add_f32_e32 v154, 1.0, v154
	v_rcp_f32_e32 v154, v154
	v_add_f32_e32 v153, 1.0, v153
	v_rcp_f32_e32 v153, v153
	v_fma_f32 v154, v154, v170, v97
	v_log_f32_e32 v178, v154
	v_fmac_f32_e32 v97, v153, v170
	v_log_f32_e32 v153, v97
	v_add_f32_e32 v186, v178, v185
	v_add_f32_e32 v153, v153, v186
	ds_write_b32 v85, v153
	s_waitcnt lgkmcnt(0)
	s_barrier
	ds_read2st64_b32 v[178:179], v87 offset1:2
	s_waitcnt lgkmcnt(0)
	v_add_f32_e32 v170, 0, v178
	v_cndmask_b32_e64 v170, v170, 0, s[4:5]
	v_add_f32_e32 v178, v179, v170
	v_cndmask_b32_e64 v170, v170, v178, s[6:7]
	ds_read2st64_b32 v[178:179], v87 offset0:4 offset1:6
	s_waitcnt lgkmcnt(0)
	v_add_f32_e32 v178, v178, v170
	v_cndmask_b32_e64 v170, v170, v178, s[8:9]
	v_add_f32_e32 v178, v179, v170
	v_cndmask_b32_e64 v178, v170, v178, s[10:11]
	v_add_f32_e32 v179, v166, v178
	v_add_f32_e32 v187, v172, v178
	v_add_f32_e32 v188, v173, v178
	v_add_f32_e32 v189, v174, v178
	v_add_f32_e32 v192, v178, v175
	v_add_f32_e32 v193, v178, v176
	v_add_f32_e32 v177, v178, v177
	v_add_f32_e32 v176, v178, v157
	v_add_f32_e32 v175, v178, v180
	v_add_f32_e32 v174, v178, v181
	v_add_f32_e32 v173, v178, v182
	v_add_f32_e32 v172, v178, v183
	v_add_f32_e32 v170, v178, v184
	v_add_f32_e32 v166, v178, v185
	v_add_f32_e32 v157, v178, v186
	v_add_f32_e32 v153, v178, v153
	v_lshlrev_b32_e32 v178, 16, v152
	v_mul_f32_e32 v180, 0xbfb8aa3b, v178
	v_exp_f32_e32 v180, v180
	v_and_b32_e32 v152, 0xffff0000, v152
	v_add_f32_e32 v180, 1.0, v180
	v_rcp_f32_e32 v180, v180
	s_nop 0
	v_mul_f32_e32 v178, v180, v178
	v_exp_f32_e32 v180, v179
	v_exp_f32_e64 v179, -v179
	v_mul_f32_e32 v178, v178, v180
	v_mul_f32_e32 v167, v167, v179
	v_cvt_pk_bf16_f32 v178, v178, v75
	ds_write_b16 v89, v178
	v_cvt_pk_bf16_f32 v167, v167, v75
	ds_write_b16 v89, v167 offset:17408
	v_mul_f32_e32 v167, 0xbfb8aa3b, v152
	v_exp_f32_e32 v167, v167
	s_nop 0
	v_add_f32_e32 v167, 1.0, v167
	v_rcp_f32_e32 v167, v167
	s_nop 0
	v_mul_f32_e32 v152, v167, v152
	v_exp_f32_e32 v167, v187
	s_nop 0
	v_mul_f32_e32 v152, v152, v167
	v_exp_f32_e64 v167, -v187
	v_cvt_pk_bf16_f32 v152, v152, v75
	ds_write_b16 v89, v152 offset:272
	v_mul_f32_e32 v165, v165, v167
	v_cvt_pk_bf16_f32 v152, v165, v75
	ds_write_b16 v89, v152 offset:17680
	v_lshlrev_b32_e32 v152, 16, v151
	v_mul_f32_e32 v165, 0xbfb8aa3b, v152
	v_exp_f32_e32 v165, v165
	v_and_b32_e32 v151, 0xffff0000, v151
	v_add_f32_e32 v165, 1.0, v165
	v_rcp_f32_e32 v165, v165
	s_nop 0
	v_mul_f32_e32 v152, v165, v152
	v_exp_f32_e32 v165, v188
	s_nop 0
	v_mul_f32_e32 v152, v152, v165
	v_exp_f32_e64 v165, -v188
	v_cvt_pk_bf16_f32 v152, v152, v75
	ds_write_b16 v89, v152 offset:544
	v_mul_f32_e32 v163, v163, v165
	v_cvt_pk_bf16_f32 v152, v163, v75
	ds_write_b16 v89, v152 offset:17952
	v_mul_f32_e32 v152, 0xbfb8aa3b, v151
	v_exp_f32_e32 v152, v152
	s_nop 0
	v_add_f32_e32 v152, 1.0, v152
	v_rcp_f32_e32 v152, v152
	s_nop 0
	v_mul_f32_e32 v151, v152, v151
	v_exp_f32_e32 v152, v189
	s_nop 0
	v_mul_f32_e32 v151, v151, v152
	v_sub_f32_e32 v152, 1.0, v161
	v_exp_f32_e64 v161, -v189
	v_cvt_pk_bf16_f32 v151, v151, v75
	ds_write_b16 v89, v151 offset:816
	v_mul_f32_e32 v152, v152, v161
	v_cvt_pk_bf16_f32 v151, v152, v75
	ds_write_b16 v89, v151 offset:18224
	v_lshlrev_b32_e32 v151, 16, v150
	v_mul_f32_e32 v152, 0xbfb8aa3b, v151
	v_exp_f32_e32 v152, v152
	v_and_b32_e32 v150, 0xffff0000, v150
	v_add_f32_e32 v152, 1.0, v152
	v_rcp_f32_e32 v152, v152
	s_nop 0
	v_mul_f32_e32 v151, v152, v151
	v_exp_f32_e32 v152, v192
	s_nop 0
	v_mul_f32_e32 v151, v151, v152
	v_sub_f32_e32 v152, 1.0, v160
	v_exp_f32_e64 v160, -v192
	v_cvt_pk_bf16_f32 v151, v151, v75
	ds_write_b16 v89, v151 offset:1088
	v_mul_f32_e32 v152, v152, v160
	v_cvt_pk_bf16_f32 v151, v152, v75
	ds_write_b16 v89, v151 offset:18496
	v_mul_f32_e32 v151, 0xbfb8aa3b, v150
	v_exp_f32_e32 v151, v151
	v_exp_f32_e64 v152, -v193
	v_add_f32_e32 v151, 1.0, v151
	v_rcp_f32_e32 v151, v151
	s_nop 0
	v_mul_f32_e32 v150, v151, v150
	v_exp_f32_e32 v151, v193
	s_nop 0
	v_mul_f32_e32 v150, v150, v151
	v_sub_f32_e32 v151, 1.0, v158
	v_cvt_pk_bf16_f32 v150, v150, v75
	v_mul_f32_e32 v151, v151, v152
	ds_write_b16 v89, v150 offset:1360
	v_cvt_pk_bf16_f32 v150, v151, v75
	ds_write_b16 v89, v150 offset:18768
	v_lshlrev_b32_e32 v150, 16, v149
	v_mul_f32_e32 v151, 0xbfb8aa3b, v150
	v_exp_f32_e32 v151, v151
	v_exp_f32_e64 v152, -v177
	v_and_b32_e32 v149, 0xffff0000, v149
	v_add_f32_e32 v151, 1.0, v151
	v_rcp_f32_e32 v151, v151
	s_nop 0
	v_mul_f32_e32 v150, v151, v150
	v_exp_f32_e32 v151, v177
	s_nop 0
	v_mul_f32_e32 v150, v150, v151
	v_sub_f32_e32 v151, 1.0, v159
	v_cvt_pk_bf16_f32 v150, v150, v75
	v_mul_f32_e32 v151, v151, v152
	ds_write_b16 v89, v150 offset:1632
	v_cvt_pk_bf16_f32 v150, v151, v75
	ds_write_b16 v89, v150 offset:19040
	v_mul_f32_e32 v150, 0xbfb8aa3b, v149
	v_exp_f32_e32 v150, v150
	v_exp_f32_e64 v151, -v176
	v_add_f32_e32 v150, 1.0, v150
	v_rcp_f32_e32 v150, v150
	s_nop 0
	v_mul_f32_e32 v149, v150, v149
	v_exp_f32_e32 v150, v176
	s_nop 0
	v_mul_f32_e32 v149, v149, v150
	v_sub_f32_e32 v150, 1.0, v171
	v_cvt_pk_bf16_f32 v149, v149, v75
	v_mul_f32_e32 v150, v150, v151
	ds_write_b16 v89, v149 offset:1904
	v_cvt_pk_bf16_f32 v149, v150, v75
	ds_write_b16 v89, v149 offset:19312
	v_lshlrev_b32_e32 v149, 16, v148
	v_mul_f32_e32 v150, 0xbfb8aa3b, v149
	v_exp_f32_e32 v150, v150
	v_exp_f32_e64 v151, -v175
	v_and_b32_e32 v148, 0xffff0000, v148
	v_add_f32_e32 v150, 1.0, v150
	v_rcp_f32_e32 v150, v150
	s_nop 0
	v_mul_f32_e32 v149, v150, v149
	v_exp_f32_e32 v150, v175
	s_nop 0
	v_mul_f32_e32 v149, v149, v150
	v_sub_f32_e32 v150, 1.0, v169
	v_cvt_pk_bf16_f32 v149, v149, v75
	v_mul_f32_e32 v150, v150, v151
	ds_write_b16 v89, v149 offset:2176
	v_cvt_pk_bf16_f32 v149, v150, v75
	ds_write_b16 v89, v149 offset:19584
	v_mul_f32_e32 v149, 0xbfb8aa3b, v148
	v_exp_f32_e32 v149, v149
	v_exp_f32_e64 v150, -v174
	v_add_f32_e32 v149, 1.0, v149
	v_rcp_f32_e32 v149, v149
	s_nop 0
	v_mul_f32_e32 v148, v149, v148
	v_exp_f32_e32 v149, v174
	s_nop 0
	v_mul_f32_e32 v148, v148, v149
	v_sub_f32_e32 v149, 1.0, v168
	v_cvt_pk_bf16_f32 v148, v148, v75
	v_mul_f32_e32 v149, v149, v150
	ds_write_b16 v89, v148 offset:2448
	v_cvt_pk_bf16_f32 v148, v149, v75
	ds_write_b16 v89, v148 offset:19856
	v_lshlrev_b32_e32 v148, 16, v69
	v_mul_f32_e32 v149, 0xbfb8aa3b, v148
	v_exp_f32_e32 v149, v149
	v_exp_f32_e64 v150, -v173
	v_and_b32_e32 v69, 0xffff0000, v69
	v_add_f32_e32 v149, 1.0, v149
	v_rcp_f32_e32 v149, v149
	s_nop 0
	v_mul_f32_e32 v148, v149, v148
	v_exp_f32_e32 v149, v173
	s_nop 0
	v_mul_f32_e32 v148, v148, v149
	v_sub_f32_e32 v149, 1.0, v164
	v_cvt_pk_bf16_f32 v148, v148, v75
	v_mul_f32_e32 v149, v149, v150
	ds_write_b16 v89, v148 offset:2720
	v_cvt_pk_bf16_f32 v148, v149, v75
	ds_write_b16 v89, v148 offset:20128
	v_mul_f32_e32 v148, 0xbfb8aa3b, v69
	v_exp_f32_e32 v148, v148
	v_exp_f32_e64 v149, -v172
	v_add_f32_e32 v148, 1.0, v148
	v_rcp_f32_e32 v148, v148
	s_nop 0
	v_mul_f32_e32 v69, v148, v69
	v_exp_f32_e32 v148, v172
	s_nop 0
	v_mul_f32_e32 v69, v69, v148
	v_sub_f32_e32 v148, 1.0, v162
	v_cvt_pk_bf16_f32 v69, v69, v75
	v_mul_f32_e32 v148, v148, v149
	ds_write_b16 v89, v69 offset:2992
	v_cvt_pk_bf16_f32 v69, v148, v75
	ds_write_b16 v89, v69 offset:20400
	v_lshlrev_b32_e32 v69, 16, v68
	v_mul_f32_e32 v148, 0xbfb8aa3b, v69
	v_exp_f32_e32 v148, v148
	v_exp_f32_e64 v149, -v170
	v_and_b32_e32 v68, 0xffff0000, v68
	v_add_f32_e32 v148, 1.0, v148
	v_rcp_f32_e32 v148, v148
	s_nop 0
	v_mul_f32_e32 v69, v148, v69
	v_exp_f32_e32 v148, v170
	s_nop 0
	v_mul_f32_e32 v69, v69, v148
	v_sub_f32_e32 v148, 1.0, v156
	v_cvt_pk_bf16_f32 v69, v69, v75
	v_mul_f32_e32 v148, v148, v149
	ds_write_b16 v89, v69 offset:3264
	v_cvt_pk_bf16_f32 v69, v148, v75
	ds_write_b16 v89, v69 offset:20672
	v_mul_f32_e32 v69, 0xbfb8aa3b, v68
	v_exp_f32_e32 v69, v69
	v_exp_f32_e64 v148, -v166
	v_add_f32_e32 v69, 1.0, v69
	v_rcp_f32_e32 v69, v69
	s_nop 0
	v_mul_f32_e32 v68, v69, v68
	v_exp_f32_e32 v69, v166
	s_nop 0
	v_mul_f32_e32 v68, v68, v69
	v_sub_f32_e32 v69, 1.0, v155
	v_cvt_pk_bf16_f32 v68, v68, v75
	v_mul_f32_e32 v69, v69, v148
	ds_write_b16 v89, v68 offset:3536
	v_cvt_pk_bf16_f32 v68, v69, v75
	ds_write_b16 v89, v68 offset:20944
	v_lshlrev_b32_e32 v68, 16, v67
	v_mul_f32_e32 v69, 0xbfb8aa3b, v68
	v_exp_f32_e32 v69, v69
	v_exp_f32_e64 v148, -v157
	v_and_b32_e32 v67, 0xffff0000, v67
	v_add_f32_e32 v69, 1.0, v69
	v_rcp_f32_e32 v69, v69
	s_nop 0
	v_mul_f32_e32 v68, v69, v68
	v_exp_f32_e32 v69, v157
	s_nop 0
	v_mul_f32_e32 v68, v68, v69
	v_sub_f32_e32 v69, 1.0, v154
	v_cvt_pk_bf16_f32 v68, v68, v75
	v_mul_f32_e32 v69, v69, v148
	ds_write_b16 v89, v68 offset:3808
	v_cvt_pk_bf16_f32 v68, v69, v75
	ds_write_b16 v89, v68 offset:21216
	v_mul_f32_e32 v68, 0xbfb8aa3b, v67
	v_exp_f32_e32 v68, v68
	v_exp_f32_e64 v69, -v153
	v_add_f32_e32 v68, 1.0, v68
	v_rcp_f32_e32 v68, v68
	s_nop 0
	v_mul_f32_e32 v67, v68, v67
	v_exp_f32_e32 v68, v153
	s_nop 0
	v_mul_f32_e32 v67, v67, v68
	v_sub_f32_e32 v68, 1.0, v97
	v_cvt_pk_bf16_f32 v67, v67, v75
	v_mul_f32_e32 v68, v68, v69
	ds_write_b16 v89, v67 offset:4080
	v_cvt_pk_bf16_f32 v67, v68, v75
	ds_write_b16 v89, v67 offset:21488
	ds_write_b128 v117, v[26:29] offset:34816
	ds_write_b128 v117, v[30:33] offset:34832
	ds_write_b128 v95, v[34:37]
	ds_write_b128 v118, v[38:41] offset:62464
	ds_write_b128 v95, v[42:45] offset:17408
	ds_write_b128 v119, v[46:49] offset:62464
	v_mov_b32_e32 v26, 0
	v_mov_b32_e32 v27, 0
	v_mov_b32_e32 v28, 0
	v_mov_b32_e32 v29, 0
	s_waitcnt lgkmcnt(0)
	s_barrier
	s_cbranch_vccnz .LBB0_528
	ds_read_b128 v[26:29], v120 offset:17408
	ds_read_b128 v[30:33], v109
	s_waitcnt lgkmcnt(0)
	v_mfma_f32_16x16x32_bf16 v[26:29], v[26:29], v[30:33], 0
	ds_read_b128 v[30:33], v120 offset:17472
	ds_read_b128 v[34:37], v109 offset:64
	s_waitcnt lgkmcnt(0)
	v_mfma_f32_16x16x32_bf16 v[26:29], v[30:33], v[34:37], v[26:29]
	ds_read_b128 v[30:33], v120 offset:17536
	ds_read_b128 v[34:37], v109 offset:128
	s_waitcnt lgkmcnt(0)
	v_mfma_f32_16x16x32_bf16 v[26:29], v[30:33], v[34:37], v[26:29]
	ds_read_b128 v[30:33], v120 offset:17600
	ds_read_b128 v[34:37], v109 offset:192
	s_waitcnt lgkmcnt(0)
	v_mfma_f32_16x16x32_bf16 v[26:29], v[30:33], v[34:37], v[26:29]

.LBB0_591:
	s_or_b64 exec, exec, s[8:9]
	s_waitcnt vmcnt(0)
	buffer_inv sc1
	s_waitcnt vmcnt(0)
.LBB0_592:
	s_or_b64 exec, exec, s[0:1]
	s_waitcnt lgkmcnt(0)
	s_barrier

.LBB0_672:
	s_or_b64 exec, exec, s[8:9]
	s_waitcnt vmcnt(0)
	buffer_inv sc1
	s_waitcnt vmcnt(0)
.LBB0_673:
	s_or_b64 exec, exec, s[0:1]
	s_waitcnt lgkmcnt(0)
	s_barrier

.LBB0_818:
	s_or_b64 exec, exec, s[8:9]
	s_waitcnt vmcnt(0)
	buffer_inv sc1
	s_waitcnt vmcnt(0)
.LBB0_819:
	s_or_b64 exec, exec, s[0:1]
	s_waitcnt lgkmcnt(0)
	s_barrier

.LBB0_977:
	s_or_b64 exec, exec, s[8:9]
	s_waitcnt vmcnt(0)
	buffer_inv sc1
	s_waitcnt vmcnt(0)
.LBB0_978:
	s_or_b64 exec, exec, s[0:1]
	s_waitcnt lgkmcnt(0)
	s_barrier

.LBB0_1072:
	s_or_b64 exec, exec, s[8:9]
	s_waitcnt vmcnt(0)
	buffer_inv sc1
	s_waitcnt vmcnt(0)
.LBB0_1073:
	s_or_b64 exec, exec, s[0:1]
	s_waitcnt lgkmcnt(0)
	s_barrier

.LBB0_1161:
	s_or_b64 exec, exec, s[6:7]
	s_mov_b64 s[6:7], exec
	v_mbcnt_lo_u32_b32 v0, s6, 0
	v_mbcnt_hi_u32_b32 v0, s7, v0
	v_cmp_eq_u32_e32 vcc, 0, v0
	s_and_saveexec_b64 s[8:9], vcc
	s_cbranch_execz .LBB0_1163
	s_bcnt1_i32_b64 s3, s[6:7]
	v_mov_b32_e32 v0, 0x2000
	v_mov_b32_e32 v1, s3
	global_atomic_add v0, v1, s[4:5] offset:1024
.LBB0_1163:
	s_or_b64 exec, exec, s[8:9]
	s_waitcnt vmcnt(0)
	buffer_inv sc1
	s_waitcnt vmcnt(0)
.LBB0_1164:
	s_or_b64 exec, exec, s[0:1]
	s_waitcnt lgkmcnt(0)
	s_barrier

	.amdhsa_kernel _Z3fwd6Params
		.amdhsa_group_segment_fixed_size 0
		.amdhsa_private_segment_fixed_size 0
		.amdhsa_kernarg_size 432
		.amdhsa_user_sgpr_count 2
		.amdhsa_user_sgpr_dispatch_ptr 0
		.amdhsa_user_sgpr_queue_ptr 0
		.amdhsa_user_sgpr_kernarg_segment_ptr 1
		.amdhsa_user_sgpr_dispatch_id 0
		.amdhsa_user_sgpr_kernarg_preload_length 0
		.amdhsa_user_sgpr_kernarg_preload_offset 0
		.amdhsa_user_sgpr_private_segment_size 0
		.amdhsa_uses_dynamic_stack 0
		.amdhsa_enable_private_segment 0
		.amdhsa_system_sgpr_workgroup_id_x 1
		.amdhsa_system_sgpr_workgroup_id_y 0
		.amdhsa_system_sgpr_workgroup_id_z 0
		.amdhsa_system_sgpr_workgroup_info 0
		.amdhsa_system_vgpr_workitem_id 0
		.amdhsa_next_free_vgpr 255
		.amdhsa_next_free_sgpr 102
		.amdhsa_accum_offset 256
		.amdhsa_reserve_vcc 1
		.amdhsa_float_round_mode_32 0
		.amdhsa_float_round_mode_16_64 0
		.amdhsa_float_denorm_mode_32 3
		.amdhsa_float_denorm_mode_16_64 3
		.amdhsa_dx10_clamp 1
		.amdhsa_ieee_mode 1
		.amdhsa_fp16_overflow 0
		.amdhsa_tg_split 0
		.amdhsa_exception_fp_ieee_invalid_op 0
		.amdhsa_exception_fp_denorm_src 0
		.amdhsa_exception_fp_ieee_div_zero 0
		.amdhsa_exception_fp_ieee_overflow 0
		.amdhsa_exception_fp_ieee_underflow 0
		.amdhsa_exception_fp_ieee_inexact 0
		.amdhsa_exception_int_div_zero 0
	.end_amdhsa_kernel

amdhsa.kernels:
  - .agpr_count:     0
    .args:
      - .offset:         0
        .size:           176
        .value_kind:     by_value
      - .offset:         176
        .size:           4
        .value_kind:     hidden_block_count_x
      - .offset:         180
        .size:           4
        .value_kind:     hidden_block_count_y
      - .offset:         184
        .size:           4
        .value_kind:     hidden_block_count_z
      - .offset:         188
        .size:           2
        .value_kind:     hidden_group_size_x
      - .offset:         190
        .size:           2
        .value_kind:     hidden_group_size_y
      - .offset:         192
        .size:           2
        .value_kind:     hidden_group_size_z
      - .offset:         194
        .size:           2
        .value_kind:     hidden_remainder_x
      - .offset:         196
        .size:           2
        .value_kind:     hidden_remainder_y
      - .offset:         198
        .size:           2
        .value_kind:     hidden_remainder_z
      - .offset:         216
        .size:           8
        .value_kind:     hidden_global_offset_x
      - .offset:         224
        .size:           8
        .value_kind:     hidden_global_offset_y
      - .offset:         232
        .size:           8
        .value_kind:     hidden_global_offset_z
      - .offset:         240
        .size:           2
        .value_kind:     hidden_grid_dims
      - .offset:         296
        .size:           4
        .value_kind:     hidden_dynamic_lds_size
    .group_segment_fixed_size: 0
    .kernarg_segment_align: 8
    .kernarg_segment_size: 432
    .language:       OpenCL C
    .language_version:
      - 2
      - 0
    .max_flat_workgroup_size: 512
    .name:           _Z3fwd6Params
    .private_segment_fixed_size: 0
    .sgpr_count:     108
    .sgpr_spill_count: 13
    .symbol:         _Z3fwd6Params.kd
    .uniform_work_group_size: 1
    .uses_dynamic_stack: false
    .vgpr_count:     255
    .vgpr_spill_count: 0
    .wavefront_size: 64
